# x14v4: slower progress polling (one refresh per ~4us per consumer workgroup)
# speedup vs baseline: 1.0358x; 1.0013x over previous
.Lx14_poll:
	s_cmp_lg_u32 s82, 0
	s_cbranch_scc1 .Lx14_test
	global_load_dword v9, v4, s[20:21] sc1
	global_load_dword v152, v4, s[20:21] offset:128 sc1
	s_waitcnt vmcnt(0)
	ds_write_b32 v4, v9
	ds_write_b32 v4, v152 offset:128
	s_waitcnt lgkmcnt(0)
	s_sleep 96
